# P8 SwiGLU epilogue rewritten by hand with packed-f32 math (row-scale and descale folded into one pk_fma, 710 instead of ~1080 instructions), on top of unit-top deferral and attention read pipelining
# speedup vs baseline: 1.0225x; 1.0126x over previous
;     __device__ __forceinline__ void operator()(const f32x4 (&acc)[2][2][4][2], const Unit& u, int wr, int wc, int fr, int fq) const {
;         const int row0 = u.pm * BM + wr * 64 + fr, col = u.pn * 128 + wc * 32 + 8 * fq;
;         const float* bg = bgu + (size_t)u.e * (2 * DFF) + col;
;         const f32x4 g0 = *(const f32x4*)bg, g1 = *(const f32x4*)(bg + 4), u0 = *(const f32x4*)(bg + DFF), u1 = *(const f32x4*)(bg + DFF + 4);
;         const int colw = col & ~8, odd = fq & 1;
; template <class Epi, bool GATHER, int MODE, bool SPLIT = false>
; __device__ __forceinline__ void gemm_phase(PG8_LAS unsigned char* lds, const Gemm g, const Order& S, const Epi& E) {
;     ...
;         if constexpr (MODE == 2) {
; #pragma unroll
;             for (int a = 0; a < 2; ++a)
; #pragma unroll
;                 for (int m = 0; m < 4; ++m) { const float rs = __builtin_bit_cast(float, __builtin_amdgcn_ds_bpermute((m * 16 + fr) * 4, __builtin_bit_cast(int, rs2[a])));
; #pragma unroll
;                     for (int b = 0; b < 2; ++b)
; #pragma unroll
;                         for (int n = 0; n < 2; ++n) { const v4i_t iv = __builtin_bit_cast(v4i_t, acc[a][b][m][n]); acc[a][b][m][n] = (f32x4){(float)iv[0], (float)iv[1], (float)iv[2], (float)iv[3]} * rs; } }
;         }
.LBB0_805:
	s_waitcnt vmcnt(0)
	s_nop 7
	ds_bpermute_b32 v194, v170, v165
	ds_bpermute_b32 v196, v174, v165
	ds_bpermute_b32 v198, v175, v165
	ds_bpermute_b32 v200, v176, v165
	ds_bpermute_b32 v202, v170, v188
	ds_bpermute_b32 v204, v174, v188
	ds_bpermute_b32 v206, v175, v188
	ds_bpermute_b32 v208, v176, v188
	s_lshl_b32 s0, s0, 7
	s_mov_b32 s98, 0xc01d265f
	v_ashrrev_i32_e32 v149, 31, v164
	v_mov_b32_e32 v148, v164
	v_or_b32_e32 v150, s0, v177
	v_lshlrev_b64 v[148:149], 14, v[148:149]
	v_ashrrev_i32_e32 v151, 31, v150
	v_lshl_add_u64 v[148:149], s[84:85], 0, v[148:149]
	v_lshl_add_u64 v[148:149], v[150:151], 2, v[148:149]
	v_lshl_add_u64 v[150:151], v[148:149], 0, s[24:25]
	global_load_dwordx4 v[132:135], v[148:149], off
	global_load_dwordx4 v[136:139], v[148:149], off offset:16
	global_load_dwordx4 v[140:143], v[150:151], off
	global_load_dwordx4 v[144:147], v[150:151], off offset:16
	v_bitop3_b32 v234, s0, -16, v177 bitop3:0xc8
	v_add_u32_e32 v232, s1, v169
	v_ashrrev_i32_e32 v235, 31, v234
	v_add_u32_e32 v233, 0x80, v232
	v_cvt_f32_i32_e32 v126, v126
	v_cvt_f32_i32_e32 v127, v127
	v_cvt_f32_i32_e32 v128, v128
	v_cvt_f32_i32_e32 v129, v129
	v_cvt_f32_i32_e32 v122, v122
	v_cvt_f32_i32_e32 v123, v123
	v_cvt_f32_i32_e32 v124, v124
	v_cvt_f32_i32_e32 v125, v125
	v_cvt_f32_i32_e32 v118, v118
	v_cvt_f32_i32_e32 v119, v119
	v_cvt_f32_i32_e32 v120, v120
	v_cvt_f32_i32_e32 v121, v121
	v_cvt_f32_i32_e32 v106, v106
	v_cvt_f32_i32_e32 v107, v107
	v_cvt_f32_i32_e32 v108, v108
	v_cvt_f32_i32_e32 v109, v109
	v_cvt_f32_i32_e32 v102, v102
	v_cvt_f32_i32_e32 v103, v103
	v_cvt_f32_i32_e32 v104, v104
	v_cvt_f32_i32_e32 v105, v105
	v_cvt_f32_i32_e32 v90, v90
	v_cvt_f32_i32_e32 v91, v91
	v_cvt_f32_i32_e32 v92, v92
	v_cvt_f32_i32_e32 v93, v93
	v_cvt_f32_i32_e32 v86, v86
	v_cvt_f32_i32_e32 v87, v87
	v_cvt_f32_i32_e32 v88, v88
	v_cvt_f32_i32_e32 v89, v89
	v_cvt_f32_i32_e32 v74, v74
	v_cvt_f32_i32_e32 v75, v75
	v_cvt_f32_i32_e32 v76, v76
	v_cvt_f32_i32_e32 v77, v77
	v_cvt_f32_i32_e32 v114, v114
	v_cvt_f32_i32_e32 v115, v115
	v_cvt_f32_i32_e32 v116, v116
	v_cvt_f32_i32_e32 v117, v117
	v_cvt_f32_i32_e32 v110, v110
	v_cvt_f32_i32_e32 v111, v111
	v_cvt_f32_i32_e32 v112, v112
	v_cvt_f32_i32_e32 v113, v113
	v_cvt_f32_i32_e32 v98, v98
	v_cvt_f32_i32_e32 v99, v99
	v_cvt_f32_i32_e32 v100, v100
	v_cvt_f32_i32_e32 v101, v101
	v_cvt_f32_i32_e32 v94, v94
	v_cvt_f32_i32_e32 v95, v95
	v_cvt_f32_i32_e32 v96, v96
	v_cvt_f32_i32_e32 v97, v97
	v_cvt_f32_i32_e32 v82, v82
	v_cvt_f32_i32_e32 v83, v83
	v_cvt_f32_i32_e32 v84, v84
	v_cvt_f32_i32_e32 v85, v85
	v_cvt_f32_i32_e32 v78, v78
	v_cvt_f32_i32_e32 v79, v79
	v_cvt_f32_i32_e32 v80, v80
	v_cvt_f32_i32_e32 v81, v81
	v_cvt_f32_i32_e32 v70, v70
	v_cvt_f32_i32_e32 v71, v71
	v_cvt_f32_i32_e32 v72, v72
	v_cvt_f32_i32_e32 v73, v73
	v_cvt_f32_i32_e32 v66, v66
	v_cvt_f32_i32_e32 v67, v67
	v_cvt_f32_i32_e32 v68, v68
	v_cvt_f32_i32_e32 v69, v69
	v_cvt_f32_i32_e32 v62, v62
	v_cvt_f32_i32_e32 v63, v63
	v_cvt_f32_i32_e32 v64, v64
	v_cvt_f32_i32_e32 v65, v65
	v_cvt_f32_i32_e32 v58, v58
	v_cvt_f32_i32_e32 v59, v59
	v_cvt_f32_i32_e32 v60, v60
	v_cvt_f32_i32_e32 v61, v61
	v_cvt_f32_i32_e32 v46, v46
	v_cvt_f32_i32_e32 v47, v47
	v_cvt_f32_i32_e32 v48, v48
	v_cvt_f32_i32_e32 v49, v49
	v_cvt_f32_i32_e32 v42, v42
	v_cvt_f32_i32_e32 v43, v43
	v_cvt_f32_i32_e32 v44, v44
	v_cvt_f32_i32_e32 v45, v45
	v_cvt_f32_i32_e32 v38, v38
	v_cvt_f32_i32_e32 v39, v39
	v_cvt_f32_i32_e32 v40, v40
	v_cvt_f32_i32_e32 v41, v41
	v_cvt_f32_i32_e32 v34, v34
	v_cvt_f32_i32_e32 v35, v35
	v_cvt_f32_i32_e32 v36, v36
	v_cvt_f32_i32_e32 v37, v37
	v_cvt_f32_i32_e32 v22, v22
	v_cvt_f32_i32_e32 v23, v23
	v_cvt_f32_i32_e32 v24, v24
	v_cvt_f32_i32_e32 v25, v25
	v_cvt_f32_i32_e32 v18, v18
	v_cvt_f32_i32_e32 v19, v19
	v_cvt_f32_i32_e32 v20, v20
	v_cvt_f32_i32_e32 v21, v21
	v_cvt_f32_i32_e32 v54, v54
	v_cvt_f32_i32_e32 v55, v55
	v_cvt_f32_i32_e32 v56, v56
	v_cvt_f32_i32_e32 v57, v57
	v_cvt_f32_i32_e32 v50, v50
	v_cvt_f32_i32_e32 v51, v51
	v_cvt_f32_i32_e32 v52, v52
	v_cvt_f32_i32_e32 v53, v53
	v_cvt_f32_i32_e32 v30, v30
	v_cvt_f32_i32_e32 v31, v31
	v_cvt_f32_i32_e32 v32, v32
	v_cvt_f32_i32_e32 v33, v33
	v_cvt_f32_i32_e32 v26, v26
	v_cvt_f32_i32_e32 v27, v27
	v_cvt_f32_i32_e32 v28, v28
	v_cvt_f32_i32_e32 v29, v29
	v_cvt_f32_i32_e32 v14, v14
	v_cvt_f32_i32_e32 v15, v15
	v_cvt_f32_i32_e32 v16, v16
	v_cvt_f32_i32_e32 v17, v17
	v_cvt_f32_i32_e32 v10, v10
	v_cvt_f32_i32_e32 v11, v11
	v_cvt_f32_i32_e32 v12, v12
	v_cvt_f32_i32_e32 v13, v13
	v_cvt_f32_i32_e32 v6, v6
	v_cvt_f32_i32_e32 v7, v7
	v_cvt_f32_i32_e32 v8, v8
	v_cvt_f32_i32_e32 v9, v9
	v_cvt_f32_i32_e32 v2, v2
	v_cvt_f32_i32_e32 v3, v3
	v_cvt_f32_i32_e32 v4, v4
	v_cvt_f32_i32_e32 v5, v5
	s_waitcnt lgkmcnt(0)
	v_mul_f32_e32 v194, 0x3a4d4011, v194
	v_mul_f32_e32 v196, 0x3a4d4011, v196
	v_mul_f32_e32 v198, 0x3a4d4011, v198
	v_mul_f32_e32 v200, 0x3a4d4011, v200
	v_mul_f32_e32 v202, 0x3a4d4011, v202
	v_mul_f32_e32 v204, 0x3a4d4011, v204
	v_mul_f32_e32 v206, 0x3a4d4011, v206
	v_mul_f32_e32 v208, 0x3a4d4011, v208
	s_waitcnt vmcnt(0)
;     __device__ __forceinline__ void operator()(const f32x4 (&acc)[2][2][4][2], const Unit& u, int wr, int wc, int fr, int fq) const {
;     ...
;                     const f32x4 gt = acc[ai][0][m][n] * descale + (n ? g1 : g0), up = acc[ai][1][m][n] * descale + (n ? u1 : u0);
; #pragma unroll
;                     for (int j = 0; j < 4; ++j) { const float g = fminf(gt[j], 7.0f), uu = fminf(fmaxf(up[j], -7.0f), 7.0f);
;                         const float sg = __builtin_amdgcn_rcpf(1.0f + __builtin_amdgcn_exp2f(g * (-1.702f * 1.4426950408889634f)));
;                         o[n][j] = (uu + 1.0f) * (g * sg) * oscale; }
;                 }
;                 w0[m] = __builtin_amdgcn_cvt_pk_fp8_f32(o[0][0], o[0][1], 0, false); w0[m] = __builtin_amdgcn_cvt_pk_fp8_f32(o[0][2], o[0][3], w0[m], true);
	v_pk_fma_f32 v[126:127], v[126:127], v[194:195], v[132:133] op_sel_hi:[1,0,1]
	v_pk_fma_f32 v[128:129], v[128:129], v[194:195], v[134:135] op_sel_hi:[1,0,1]
	v_pk_fma_f32 v[122:123], v[122:123], v[194:195], v[136:137] op_sel_hi:[1,0,1]
	v_pk_fma_f32 v[124:125], v[124:125], v[194:195], v[138:139] op_sel_hi:[1,0,1]
	v_pk_fma_f32 v[118:119], v[118:119], v[196:197], v[132:133] op_sel_hi:[1,0,1]
	v_pk_fma_f32 v[120:121], v[120:121], v[196:197], v[134:135] op_sel_hi:[1,0,1]
	v_pk_fma_f32 v[106:107], v[106:107], v[196:197], v[136:137] op_sel_hi:[1,0,1]
	v_pk_fma_f32 v[108:109], v[108:109], v[196:197], v[138:139] op_sel_hi:[1,0,1]
	v_pk_fma_f32 v[114:115], v[114:115], v[194:195], v[140:141] op_sel_hi:[1,0,1]
	v_pk_fma_f32 v[116:117], v[116:117], v[194:195], v[142:143] op_sel_hi:[1,0,1]
	v_pk_fma_f32 v[110:111], v[110:111], v[194:195], v[144:145] op_sel_hi:[1,0,1]
	v_pk_fma_f32 v[112:113], v[112:113], v[194:195], v[146:147] op_sel_hi:[1,0,1]
	v_pk_fma_f32 v[98:99], v[98:99], v[196:197], v[140:141] op_sel_hi:[1,0,1]
	v_pk_fma_f32 v[100:101], v[100:101], v[196:197], v[142:143] op_sel_hi:[1,0,1]
	v_pk_fma_f32 v[94:95], v[94:95], v[196:197], v[144:145] op_sel_hi:[1,0,1]
	v_pk_fma_f32 v[96:97], v[96:97], v[196:197], v[146:147] op_sel_hi:[1,0,1]
	v_min_f32_e32 v126, 0x40e00000, v126
	v_min_f32_e32 v127, 0x40e00000, v127
	v_min_f32_e32 v128, 0x40e00000, v128
	v_min_f32_e32 v129, 0x40e00000, v129
	v_min_f32_e32 v122, 0x40e00000, v122
	v_min_f32_e32 v123, 0x40e00000, v123
	v_min_f32_e32 v124, 0x40e00000, v124
	v_min_f32_e32 v125, 0x40e00000, v125
	v_min_f32_e32 v118, 0x40e00000, v118
	v_min_f32_e32 v119, 0x40e00000, v119
	v_min_f32_e32 v120, 0x40e00000, v120
	v_min_f32_e32 v121, 0x40e00000, v121
	v_min_f32_e32 v106, 0x40e00000, v106
	v_min_f32_e32 v107, 0x40e00000, v107
	v_min_f32_e32 v108, 0x40e00000, v108
	v_min_f32_e32 v109, 0x40e00000, v109
	v_pk_mul_f32 v[210:211], v[126:127], s[98:99] op_sel_hi:[1,0]
	v_pk_mul_f32 v[212:213], v[128:129], s[98:99] op_sel_hi:[1,0]
	v_pk_mul_f32 v[214:215], v[122:123], s[98:99] op_sel_hi:[1,0]
	v_pk_mul_f32 v[216:217], v[124:125], s[98:99] op_sel_hi:[1,0]
	v_pk_mul_f32 v[218:219], v[118:119], s[98:99] op_sel_hi:[1,0]
	v_pk_mul_f32 v[220:221], v[120:121], s[98:99] op_sel_hi:[1,0]
	v_pk_mul_f32 v[222:223], v[106:107], s[98:99] op_sel_hi:[1,0]
	v_pk_mul_f32 v[224:225], v[108:109], s[98:99] op_sel_hi:[1,0]
	v_exp_f32_e32 v210, v210
	v_exp_f32_e32 v211, v211
	v_exp_f32_e32 v212, v212
	v_exp_f32_e32 v213, v213
	v_exp_f32_e32 v214, v214
	v_exp_f32_e32 v215, v215
	v_exp_f32_e32 v216, v216
	v_exp_f32_e32 v217, v217
	v_exp_f32_e32 v218, v218
	v_exp_f32_e32 v219, v219
	v_exp_f32_e32 v220, v220
	v_exp_f32_e32 v221, v221
	v_exp_f32_e32 v222, v222
	v_exp_f32_e32 v223, v223
	v_exp_f32_e32 v224, v224
	v_exp_f32_e32 v225, v225
	v_med3_f32 v114, v114, s65, v183
	v_med3_f32 v115, v115, s65, v183
	v_med3_f32 v116, v116, s65, v183
	v_med3_f32 v117, v117, s65, v183
	v_med3_f32 v110, v110, s65, v183
	v_med3_f32 v111, v111, s65, v183
	v_med3_f32 v112, v112, s65, v183
	v_med3_f32 v113, v113, s65, v183
	v_med3_f32 v98, v98, s65, v183
	v_med3_f32 v99, v99, s65, v183
	v_med3_f32 v100, v100, s65, v183
	v_med3_f32 v101, v101, s65, v183
	v_med3_f32 v94, v94, s65, v183
	v_med3_f32 v95, v95, s65, v183
	v_med3_f32 v96, v96, s65, v183
	v_med3_f32 v97, v97, s65, v183
	v_pk_add_f32 v[210:211], v[210:211], 1.0 op_sel_hi:[1,0]
	v_pk_add_f32 v[212:213], v[212:213], 1.0 op_sel_hi:[1,0]
	v_pk_add_f32 v[214:215], v[214:215], 1.0 op_sel_hi:[1,0]
	v_pk_add_f32 v[216:217], v[216:217], 1.0 op_sel_hi:[1,0]
	v_pk_add_f32 v[218:219], v[218:219], 1.0 op_sel_hi:[1,0]
	v_pk_add_f32 v[220:221], v[220:221], 1.0 op_sel_hi:[1,0]
	v_pk_add_f32 v[222:223], v[222:223], 1.0 op_sel_hi:[1,0]
	v_pk_add_f32 v[224:225], v[224:225], 1.0 op_sel_hi:[1,0]
	v_rcp_f32_e32 v210, v210
	v_rcp_f32_e32 v211, v211
	v_rcp_f32_e32 v212, v212
	v_rcp_f32_e32 v213, v213
	v_rcp_f32_e32 v214, v214
	v_rcp_f32_e32 v215, v215
	v_rcp_f32_e32 v216, v216
	v_rcp_f32_e32 v217, v217
	v_rcp_f32_e32 v218, v218
	v_rcp_f32_e32 v219, v219
	v_rcp_f32_e32 v220, v220
	v_rcp_f32_e32 v221, v221
	v_rcp_f32_e32 v222, v222
	v_rcp_f32_e32 v223, v223
	v_rcp_f32_e32 v224, v224
	v_rcp_f32_e32 v225, v225
	v_pk_fma_f32 v[114:115], v[114:115], 4.0, 4.0 op_sel_hi:[1,0,0]
	v_pk_fma_f32 v[116:117], v[116:117], 4.0, 4.0 op_sel_hi:[1,0,0]
	v_pk_fma_f32 v[110:111], v[110:111], 4.0, 4.0 op_sel_hi:[1,0,0]
	v_pk_fma_f32 v[112:113], v[112:113], 4.0, 4.0 op_sel_hi:[1,0,0]
	v_pk_fma_f32 v[98:99], v[98:99], 4.0, 4.0 op_sel_hi:[1,0,0]
	v_pk_fma_f32 v[100:101], v[100:101], 4.0, 4.0 op_sel_hi:[1,0,0]
	v_pk_fma_f32 v[94:95], v[94:95], 4.0, 4.0 op_sel_hi:[1,0,0]
	v_pk_fma_f32 v[96:97], v[96:97], 4.0, 4.0 op_sel_hi:[1,0,0]
	v_pk_mul_f32 v[126:127], v[126:127], v[210:211]
	v_pk_mul_f32 v[128:129], v[128:129], v[212:213]
	v_pk_mul_f32 v[122:123], v[122:123], v[214:215]
	v_pk_mul_f32 v[124:125], v[124:125], v[216:217]
	v_pk_mul_f32 v[118:119], v[118:119], v[218:219]
	v_pk_mul_f32 v[120:121], v[120:121], v[220:221]
	v_pk_mul_f32 v[106:107], v[106:107], v[222:223]
	v_pk_mul_f32 v[108:109], v[108:109], v[224:225]
	v_pk_mul_f32 v[126:127], v[126:127], v[114:115]
	v_pk_mul_f32 v[128:129], v[128:129], v[116:117]
	v_pk_mul_f32 v[122:123], v[122:123], v[110:111]
	v_pk_mul_f32 v[124:125], v[124:125], v[112:113]
	v_pk_mul_f32 v[118:119], v[118:119], v[98:99]
	v_pk_mul_f32 v[120:121], v[120:121], v[100:101]
	v_pk_mul_f32 v[106:107], v[106:107], v[94:95]
	v_pk_mul_f32 v[108:109], v[108:109], v[96:97]
	v_cvt_pk_fp8_f32 v226, v126, v127
	v_cvt_pk_fp8_f32 v226, v128, v129 op_sel:[0,0,1]
	v_cvt_pk_fp8_f32 v227, v122, v123
	v_cvt_pk_fp8_f32 v227, v124, v125 op_sel:[0,0,1]
; __device__ __forceinline__ void swap16(int& x, int& y) { const auto r = __builtin_amdgcn_permlane16_swap((unsigned)x, (unsigned)y, false, false); x = (int)r[0]; y = (int)r[1]; }
;     __device__ __forceinline__ void operator()(const f32x4 (&acc)[2][2][4][2], const Unit& u, int wr, int wc, int fr, int fq) const {
;     ...
;                     const f32x4 gt = acc[ai][0][m][n] * descale + (n ? g1 : g0), up = acc[ai][1][m][n] * descale + (n ? u1 : u0);
; #pragma unroll
;                     for (int j = 0; j < 4; ++j) { const float g = fminf(gt[j], 7.0f), uu = fminf(fmaxf(up[j], -7.0f), 7.0f);
;                         const float sg = __builtin_amdgcn_rcpf(1.0f + __builtin_amdgcn_exp2f(g * (-1.702f * 1.4426950408889634f)));
;                         o[n][j] = (uu + 1.0f) * (g * sg) * oscale; }
;     ...
;                 w0[m] = __builtin_amdgcn_cvt_pk_fp8_f32(o[0][0], o[0][1], 0, false); w0[m] = __builtin_amdgcn_cvt_pk_fp8_f32(o[0][2], o[0][3], w0[m], true);
;                 w1[m] = __builtin_amdgcn_cvt_pk_fp8_f32(o[1][0], o[1][1], 0, false); w1[m] = __builtin_amdgcn_cvt_pk_fp8_f32(o[1][2], o[1][3], w1[m], true);
;             }
; #pragma unroll
;             for (int p = 0; p < 2; ++p) { swap16(w0[2 * p], w0[2 * p + 1]); swap16(w1[2 * p], w1[2 * p + 1]);
;                 u32x4 w; w.x = (unsigned)w0[2 * p]; w.y = (unsigned)w1[2 * p]; w.z = (unsigned)w0[2 * p + 1]; w.w = (unsigned)w1[2 * p + 1];
;                 *(u32x4*)(ACT + (size_t)(row0 + ai * HALF + (2 * p + odd) * 16) * DFF + colw) = w; }
	v_cvt_pk_fp8_f32 v228, v118, v119
	v_cvt_pk_fp8_f32 v228, v120, v121 op_sel:[0,0,1]
	v_cvt_pk_fp8_f32 v229, v106, v107
	v_cvt_pk_fp8_f32 v229, v108, v109 op_sel:[0,0,1]
	v_or_b32_e32 v230, v232, v172
	v_ashrrev_i32_e32 v231, 31, v230
	v_lshlrev_b64 v[230:231], 11, v[230:231]
	v_permlane16_swap_b32_e32 v226, v228
	v_permlane16_swap_b32_e32 v227, v229
	v_lshl_add_u64 v[230:231], s[16:17], 0, v[230:231]
	v_lshl_add_u64 v[230:231], v[230:231], 0, v[234:235]
	global_store_dwordx4 v[230:231], v[226:229], off
	v_pk_fma_f32 v[102:103], v[102:103], v[198:199], v[132:133] op_sel_hi:[1,0,1]
	v_pk_fma_f32 v[104:105], v[104:105], v[198:199], v[134:135] op_sel_hi:[1,0,1]
	v_pk_fma_f32 v[90:91], v[90:91], v[198:199], v[136:137] op_sel_hi:[1,0,1]
	v_pk_fma_f32 v[92:93], v[92:93], v[198:199], v[138:139] op_sel_hi:[1,0,1]
	v_pk_fma_f32 v[86:87], v[86:87], v[200:201], v[132:133] op_sel_hi:[1,0,1]
	v_pk_fma_f32 v[88:89], v[88:89], v[200:201], v[134:135] op_sel_hi:[1,0,1]
	v_pk_fma_f32 v[74:75], v[74:75], v[200:201], v[136:137] op_sel_hi:[1,0,1]
	v_pk_fma_f32 v[76:77], v[76:77], v[200:201], v[138:139] op_sel_hi:[1,0,1]
	v_pk_fma_f32 v[82:83], v[82:83], v[198:199], v[140:141] op_sel_hi:[1,0,1]
	v_pk_fma_f32 v[84:85], v[84:85], v[198:199], v[142:143] op_sel_hi:[1,0,1]
	v_pk_fma_f32 v[78:79], v[78:79], v[198:199], v[144:145] op_sel_hi:[1,0,1]
	v_pk_fma_f32 v[80:81], v[80:81], v[198:199], v[146:147] op_sel_hi:[1,0,1]
	v_pk_fma_f32 v[70:71], v[70:71], v[200:201], v[140:141] op_sel_hi:[1,0,1]
	v_pk_fma_f32 v[72:73], v[72:73], v[200:201], v[142:143] op_sel_hi:[1,0,1]
	v_pk_fma_f32 v[66:67], v[66:67], v[200:201], v[144:145] op_sel_hi:[1,0,1]
	v_pk_fma_f32 v[68:69], v[68:69], v[200:201], v[146:147] op_sel_hi:[1,0,1]
	v_min_f32_e32 v102, 0x40e00000, v102
	v_min_f32_e32 v103, 0x40e00000, v103
	v_min_f32_e32 v104, 0x40e00000, v104
	v_min_f32_e32 v105, 0x40e00000, v105
	v_min_f32_e32 v90, 0x40e00000, v90
	v_min_f32_e32 v91, 0x40e00000, v91
	v_min_f32_e32 v92, 0x40e00000, v92
	v_min_f32_e32 v93, 0x40e00000, v93
	v_min_f32_e32 v86, 0x40e00000, v86
	v_min_f32_e32 v87, 0x40e00000, v87
	v_min_f32_e32 v88, 0x40e00000, v88
	v_min_f32_e32 v89, 0x40e00000, v89
	v_min_f32_e32 v74, 0x40e00000, v74
	v_min_f32_e32 v75, 0x40e00000, v75
	v_min_f32_e32 v76, 0x40e00000, v76
	v_min_f32_e32 v77, 0x40e00000, v77
	v_pk_mul_f32 v[210:211], v[102:103], s[98:99] op_sel_hi:[1,0]
	v_pk_mul_f32 v[212:213], v[104:105], s[98:99] op_sel_hi:[1,0]
	v_pk_mul_f32 v[214:215], v[90:91], s[98:99] op_sel_hi:[1,0]
	v_pk_mul_f32 v[216:217], v[92:93], s[98:99] op_sel_hi:[1,0]
	v_pk_mul_f32 v[218:219], v[86:87], s[98:99] op_sel_hi:[1,0]
	v_pk_mul_f32 v[220:221], v[88:89], s[98:99] op_sel_hi:[1,0]
	v_pk_mul_f32 v[222:223], v[74:75], s[98:99] op_sel_hi:[1,0]
	v_pk_mul_f32 v[224:225], v[76:77], s[98:99] op_sel_hi:[1,0]
	v_exp_f32_e32 v210, v210
	v_exp_f32_e32 v211, v211
	v_exp_f32_e32 v212, v212
	v_exp_f32_e32 v213, v213
	v_exp_f32_e32 v214, v214
	v_exp_f32_e32 v215, v215
	v_exp_f32_e32 v216, v216
	v_exp_f32_e32 v217, v217
	v_exp_f32_e32 v218, v218
	v_exp_f32_e32 v219, v219
	v_exp_f32_e32 v220, v220
	v_exp_f32_e32 v221, v221
	v_exp_f32_e32 v222, v222
	v_exp_f32_e32 v223, v223
	v_exp_f32_e32 v224, v224
	v_exp_f32_e32 v225, v225
	v_med3_f32 v82, v82, s65, v183
	v_med3_f32 v83, v83, s65, v183
	v_med3_f32 v84, v84, s65, v183
	v_med3_f32 v85, v85, s65, v183
	v_med3_f32 v78, v78, s65, v183
	v_med3_f32 v79, v79, s65, v183
	v_med3_f32 v80, v80, s65, v183
	v_med3_f32 v81, v81, s65, v183
	v_med3_f32 v70, v70, s65, v183
	v_med3_f32 v71, v71, s65, v183
	v_med3_f32 v72, v72, s65, v183
	v_med3_f32 v73, v73, s65, v183
	v_med3_f32 v66, v66, s65, v183
	v_med3_f32 v67, v67, s65, v183
	v_med3_f32 v68, v68, s65, v183
	v_med3_f32 v69, v69, s65, v183
	v_pk_add_f32 v[210:211], v[210:211], 1.0 op_sel_hi:[1,0]
	v_pk_add_f32 v[212:213], v[212:213], 1.0 op_sel_hi:[1,0]
	v_pk_add_f32 v[214:215], v[214:215], 1.0 op_sel_hi:[1,0]
	v_pk_add_f32 v[216:217], v[216:217], 1.0 op_sel_hi:[1,0]
	v_pk_add_f32 v[218:219], v[218:219], 1.0 op_sel_hi:[1,0]
	v_pk_add_f32 v[220:221], v[220:221], 1.0 op_sel_hi:[1,0]
	v_pk_add_f32 v[222:223], v[222:223], 1.0 op_sel_hi:[1,0]
	v_pk_add_f32 v[224:225], v[224:225], 1.0 op_sel_hi:[1,0]
	v_rcp_f32_e32 v210, v210
	v_rcp_f32_e32 v211, v211
	v_rcp_f32_e32 v212, v212
	v_rcp_f32_e32 v213, v213
	v_rcp_f32_e32 v214, v214
	v_rcp_f32_e32 v215, v215
	v_rcp_f32_e32 v216, v216
	v_rcp_f32_e32 v217, v217
	v_rcp_f32_e32 v218, v218
	v_rcp_f32_e32 v219, v219
	v_rcp_f32_e32 v220, v220
	v_rcp_f32_e32 v221, v221
	v_rcp_f32_e32 v222, v222
	v_rcp_f32_e32 v223, v223
	v_rcp_f32_e32 v224, v224
	v_rcp_f32_e32 v225, v225
	v_pk_fma_f32 v[82:83], v[82:83], 4.0, 4.0 op_sel_hi:[1,0,0]
	v_pk_fma_f32 v[84:85], v[84:85], 4.0, 4.0 op_sel_hi:[1,0,0]
	v_pk_fma_f32 v[78:79], v[78:79], 4.0, 4.0 op_sel_hi:[1,0,0]
	v_pk_fma_f32 v[80:81], v[80:81], 4.0, 4.0 op_sel_hi:[1,0,0]
	v_pk_fma_f32 v[70:71], v[70:71], 4.0, 4.0 op_sel_hi:[1,0,0]
	v_pk_fma_f32 v[72:73], v[72:73], 4.0, 4.0 op_sel_hi:[1,0,0]
	v_pk_fma_f32 v[66:67], v[66:67], 4.0, 4.0 op_sel_hi:[1,0,0]
	v_pk_fma_f32 v[68:69], v[68:69], 4.0, 4.0 op_sel_hi:[1,0,0]
	v_pk_mul_f32 v[102:103], v[102:103], v[210:211]
	v_pk_mul_f32 v[104:105], v[104:105], v[212:213]
	v_pk_mul_f32 v[90:91], v[90:91], v[214:215]
	v_pk_mul_f32 v[92:93], v[92:93], v[216:217]
	v_pk_mul_f32 v[86:87], v[86:87], v[218:219]
	v_pk_mul_f32 v[88:89], v[88:89], v[220:221]
	v_pk_mul_f32 v[74:75], v[74:75], v[222:223]
	v_pk_mul_f32 v[76:77], v[76:77], v[224:225]
	v_pk_mul_f32 v[102:103], v[102:103], v[82:83]
	v_pk_mul_f32 v[104:105], v[104:105], v[84:85]
	v_pk_mul_f32 v[90:91], v[90:91], v[78:79]
	v_pk_mul_f32 v[92:93], v[92:93], v[80:81]
; __device__ __forceinline__ void swap16(int& x, int& y) { const auto r = __builtin_amdgcn_permlane16_swap((unsigned)x, (unsigned)y, false, false); x = (int)r[0]; y = (int)r[1]; }
;     __device__ __forceinline__ void operator()(const f32x4 (&acc)[2][2][4][2], const Unit& u, int wr, int wc, int fr, int fq) const {
;     ...
;                     const f32x4 gt = acc[ai][0][m][n] * descale + (n ? g1 : g0), up = acc[ai][1][m][n] * descale + (n ? u1 : u0);
; #pragma unroll
;                     for (int j = 0; j < 4; ++j) { const float g = fminf(gt[j], 7.0f), uu = fminf(fmaxf(up[j], -7.0f), 7.0f);
;                         const float sg = __builtin_amdgcn_rcpf(1.0f + __builtin_amdgcn_exp2f(g * (-1.702f * 1.4426950408889634f)));
;                         o[n][j] = (uu + 1.0f) * (g * sg) * oscale; }
;     ...
;                 w0[m] = __builtin_amdgcn_cvt_pk_fp8_f32(o[0][0], o[0][1], 0, false); w0[m] = __builtin_amdgcn_cvt_pk_fp8_f32(o[0][2], o[0][3], w0[m], true);
;                 w1[m] = __builtin_amdgcn_cvt_pk_fp8_f32(o[1][0], o[1][1], 0, false); w1[m] = __builtin_amdgcn_cvt_pk_fp8_f32(o[1][2], o[1][3], w1[m], true);
;             }
; #pragma unroll
;             for (int p = 0; p < 2; ++p) { swap16(w0[2 * p], w0[2 * p + 1]); swap16(w1[2 * p], w1[2 * p + 1]);
;                 u32x4 w; w.x = (unsigned)w0[2 * p]; w.y = (unsigned)w1[2 * p]; w.z = (unsigned)w0[2 * p + 1]; w.w = (unsigned)w1[2 * p + 1];
;                 *(u32x4*)(ACT + (size_t)(row0 + ai * HALF + (2 * p + odd) * 16) * DFF + colw) = w; }
	v_pk_mul_f32 v[86:87], v[86:87], v[70:71]
	v_pk_mul_f32 v[88:89], v[88:89], v[72:73]
	v_pk_mul_f32 v[74:75], v[74:75], v[66:67]
	v_pk_mul_f32 v[76:77], v[76:77], v[68:69]
	v_cvt_pk_fp8_f32 v236, v102, v103
	v_cvt_pk_fp8_f32 v236, v104, v105 op_sel:[0,0,1]
	v_cvt_pk_fp8_f32 v237, v90, v91
	v_cvt_pk_fp8_f32 v237, v92, v93 op_sel:[0,0,1]
	v_cvt_pk_fp8_f32 v238, v86, v87
	v_cvt_pk_fp8_f32 v238, v88, v89 op_sel:[0,0,1]
	v_cvt_pk_fp8_f32 v239, v74, v75
	v_cvt_pk_fp8_f32 v239, v76, v77 op_sel:[0,0,1]
	v_or_b32_e32 v230, v232, v173
	v_ashrrev_i32_e32 v231, 31, v230
	v_lshlrev_b64 v[230:231], 11, v[230:231]
	v_permlane16_swap_b32_e32 v236, v238
	v_permlane16_swap_b32_e32 v237, v239
	v_lshl_add_u64 v[230:231], s[16:17], 0, v[230:231]
	v_lshl_add_u64 v[230:231], v[230:231], 0, v[234:235]
	global_store_dwordx4 v[230:231], v[236:239], off
	v_pk_fma_f32 v[62:63], v[62:63], v[202:203], v[132:133] op_sel_hi:[1,0,1]
	v_pk_fma_f32 v[64:65], v[64:65], v[202:203], v[134:135] op_sel_hi:[1,0,1]
	v_pk_fma_f32 v[58:59], v[58:59], v[202:203], v[136:137] op_sel_hi:[1,0,1]
	v_pk_fma_f32 v[60:61], v[60:61], v[202:203], v[138:139] op_sel_hi:[1,0,1]
	v_pk_fma_f32 v[46:47], v[46:47], v[204:205], v[132:133] op_sel_hi:[1,0,1]
	v_pk_fma_f32 v[48:49], v[48:49], v[204:205], v[134:135] op_sel_hi:[1,0,1]
	v_pk_fma_f32 v[42:43], v[42:43], v[204:205], v[136:137] op_sel_hi:[1,0,1]
	v_pk_fma_f32 v[44:45], v[44:45], v[204:205], v[138:139] op_sel_hi:[1,0,1]
	v_pk_fma_f32 v[54:55], v[54:55], v[202:203], v[140:141] op_sel_hi:[1,0,1]
	v_pk_fma_f32 v[56:57], v[56:57], v[202:203], v[142:143] op_sel_hi:[1,0,1]
	v_pk_fma_f32 v[50:51], v[50:51], v[202:203], v[144:145] op_sel_hi:[1,0,1]
	v_pk_fma_f32 v[52:53], v[52:53], v[202:203], v[146:147] op_sel_hi:[1,0,1]
	v_pk_fma_f32 v[30:31], v[30:31], v[204:205], v[140:141] op_sel_hi:[1,0,1]
	v_pk_fma_f32 v[32:33], v[32:33], v[204:205], v[142:143] op_sel_hi:[1,0,1]
	v_pk_fma_f32 v[26:27], v[26:27], v[204:205], v[144:145] op_sel_hi:[1,0,1]
	v_pk_fma_f32 v[28:29], v[28:29], v[204:205], v[146:147] op_sel_hi:[1,0,1]
	v_min_f32_e32 v62, 0x40e00000, v62
	v_min_f32_e32 v63, 0x40e00000, v63
	v_min_f32_e32 v64, 0x40e00000, v64
	v_min_f32_e32 v65, 0x40e00000, v65
	v_min_f32_e32 v58, 0x40e00000, v58
	v_min_f32_e32 v59, 0x40e00000, v59
	v_min_f32_e32 v60, 0x40e00000, v60
	v_min_f32_e32 v61, 0x40e00000, v61
	v_min_f32_e32 v46, 0x40e00000, v46
	v_min_f32_e32 v47, 0x40e00000, v47
	v_min_f32_e32 v48, 0x40e00000, v48
	v_min_f32_e32 v49, 0x40e00000, v49
	v_min_f32_e32 v42, 0x40e00000, v42
	v_min_f32_e32 v43, 0x40e00000, v43
	v_min_f32_e32 v44, 0x40e00000, v44
	v_min_f32_e32 v45, 0x40e00000, v45
	v_pk_mul_f32 v[210:211], v[62:63], s[98:99] op_sel_hi:[1,0]
	v_pk_mul_f32 v[212:213], v[64:65], s[98:99] op_sel_hi:[1,0]
	v_pk_mul_f32 v[214:215], v[58:59], s[98:99] op_sel_hi:[1,0]
	v_pk_mul_f32 v[216:217], v[60:61], s[98:99] op_sel_hi:[1,0]
	v_pk_mul_f32 v[218:219], v[46:47], s[98:99] op_sel_hi:[1,0]
	v_pk_mul_f32 v[220:221], v[48:49], s[98:99] op_sel_hi:[1,0]
	v_pk_mul_f32 v[222:223], v[42:43], s[98:99] op_sel_hi:[1,0]
	v_pk_mul_f32 v[224:225], v[44:45], s[98:99] op_sel_hi:[1,0]
	v_exp_f32_e32 v210, v210
	v_exp_f32_e32 v211, v211
	v_exp_f32_e32 v212, v212
	v_exp_f32_e32 v213, v213
	v_exp_f32_e32 v214, v214
	v_exp_f32_e32 v215, v215
	v_exp_f32_e32 v216, v216
	v_exp_f32_e32 v217, v217
	v_exp_f32_e32 v218, v218
	v_exp_f32_e32 v219, v219
	v_exp_f32_e32 v220, v220
	v_exp_f32_e32 v221, v221
	v_exp_f32_e32 v222, v222
	v_exp_f32_e32 v223, v223
	v_exp_f32_e32 v224, v224
	v_exp_f32_e32 v225, v225
	v_med3_f32 v54, v54, s65, v183
	v_med3_f32 v55, v55, s65, v183
	v_med3_f32 v56, v56, s65, v183
	v_med3_f32 v57, v57, s65, v183
	v_med3_f32 v50, v50, s65, v183
	v_med3_f32 v51, v51, s65, v183
	v_med3_f32 v52, v52, s65, v183
	v_med3_f32 v53, v53, s65, v183
	v_med3_f32 v30, v30, s65, v183
	v_med3_f32 v31, v31, s65, v183
	v_med3_f32 v32, v32, s65, v183
	v_med3_f32 v33, v33, s65, v183
	v_med3_f32 v26, v26, s65, v183
	v_med3_f32 v27, v27, s65, v183
	v_med3_f32 v28, v28, s65, v183
	v_med3_f32 v29, v29, s65, v183
	v_pk_add_f32 v[210:211], v[210:211], 1.0 op_sel_hi:[1,0]
	v_pk_add_f32 v[212:213], v[212:213], 1.0 op_sel_hi:[1,0]
	v_pk_add_f32 v[214:215], v[214:215], 1.0 op_sel_hi:[1,0]
	v_pk_add_f32 v[216:217], v[216:217], 1.0 op_sel_hi:[1,0]
	v_pk_add_f32 v[218:219], v[218:219], 1.0 op_sel_hi:[1,0]
	v_pk_add_f32 v[220:221], v[220:221], 1.0 op_sel_hi:[1,0]
	v_pk_add_f32 v[222:223], v[222:223], 1.0 op_sel_hi:[1,0]
	v_pk_add_f32 v[224:225], v[224:225], 1.0 op_sel_hi:[1,0]
	v_rcp_f32_e32 v210, v210
	v_rcp_f32_e32 v211, v211
	v_rcp_f32_e32 v212, v212
	v_rcp_f32_e32 v213, v213
	v_rcp_f32_e32 v214, v214
	v_rcp_f32_e32 v215, v215
	v_rcp_f32_e32 v216, v216
	v_rcp_f32_e32 v217, v217
	v_rcp_f32_e32 v218, v218
	v_rcp_f32_e32 v219, v219
	v_rcp_f32_e32 v220, v220
	v_rcp_f32_e32 v221, v221
	v_rcp_f32_e32 v222, v222
	v_rcp_f32_e32 v223, v223
	v_rcp_f32_e32 v224, v224
	v_rcp_f32_e32 v225, v225
	v_pk_fma_f32 v[54:55], v[54:55], 4.0, 4.0 op_sel_hi:[1,0,0]
	v_pk_fma_f32 v[56:57], v[56:57], 4.0, 4.0 op_sel_hi:[1,0,0]
	v_pk_fma_f32 v[50:51], v[50:51], 4.0, 4.0 op_sel_hi:[1,0,0]
	v_pk_fma_f32 v[52:53], v[52:53], 4.0, 4.0 op_sel_hi:[1,0,0]
	v_pk_fma_f32 v[30:31], v[30:31], 4.0, 4.0 op_sel_hi:[1,0,0]
	v_pk_fma_f32 v[32:33], v[32:33], 4.0, 4.0 op_sel_hi:[1,0,0]
	v_pk_fma_f32 v[26:27], v[26:27], 4.0, 4.0 op_sel_hi:[1,0,0]
	v_pk_fma_f32 v[28:29], v[28:29], 4.0, 4.0 op_sel_hi:[1,0,0]
	v_pk_mul_f32 v[62:63], v[62:63], v[210:211]
	v_pk_mul_f32 v[64:65], v[64:65], v[212:213]
	v_pk_mul_f32 v[58:59], v[58:59], v[214:215]
	v_pk_mul_f32 v[60:61], v[60:61], v[216:217]
	v_pk_mul_f32 v[46:47], v[46:47], v[218:219]
; __device__ __forceinline__ void swap16(int& x, int& y) { const auto r = __builtin_amdgcn_permlane16_swap((unsigned)x, (unsigned)y, false, false); x = (int)r[0]; y = (int)r[1]; }
;     __device__ __forceinline__ void operator()(const f32x4 (&acc)[2][2][4][2], const Unit& u, int wr, int wc, int fr, int fq) const {
;     ...
;                     const f32x4 gt = acc[ai][0][m][n] * descale + (n ? g1 : g0), up = acc[ai][1][m][n] * descale + (n ? u1 : u0);
; #pragma unroll
;                     for (int j = 0; j < 4; ++j) { const float g = fminf(gt[j], 7.0f), uu = fminf(fmaxf(up[j], -7.0f), 7.0f);
;                         const float sg = __builtin_amdgcn_rcpf(1.0f + __builtin_amdgcn_exp2f(g * (-1.702f * 1.4426950408889634f)));
;                         o[n][j] = (uu + 1.0f) * (g * sg) * oscale; }
;     ...
;                 w0[m] = __builtin_amdgcn_cvt_pk_fp8_f32(o[0][0], o[0][1], 0, false); w0[m] = __builtin_amdgcn_cvt_pk_fp8_f32(o[0][2], o[0][3], w0[m], true);
;                 w1[m] = __builtin_amdgcn_cvt_pk_fp8_f32(o[1][0], o[1][1], 0, false); w1[m] = __builtin_amdgcn_cvt_pk_fp8_f32(o[1][2], o[1][3], w1[m], true);
;             }
; #pragma unroll
;             for (int p = 0; p < 2; ++p) { swap16(w0[2 * p], w0[2 * p + 1]); swap16(w1[2 * p], w1[2 * p + 1]);
;                 u32x4 w; w.x = (unsigned)w0[2 * p]; w.y = (unsigned)w1[2 * p]; w.z = (unsigned)w0[2 * p + 1]; w.w = (unsigned)w1[2 * p + 1];
;                 *(u32x4*)(ACT + (size_t)(row0 + ai * HALF + (2 * p + odd) * 16) * DFF + colw) = w; }
	v_pk_mul_f32 v[48:49], v[48:49], v[220:221]
	v_pk_mul_f32 v[42:43], v[42:43], v[222:223]
	v_pk_mul_f32 v[44:45], v[44:45], v[224:225]
	v_pk_mul_f32 v[62:63], v[62:63], v[54:55]
	v_pk_mul_f32 v[64:65], v[64:65], v[56:57]
	v_pk_mul_f32 v[58:59], v[58:59], v[50:51]
	v_pk_mul_f32 v[60:61], v[60:61], v[52:53]
	v_pk_mul_f32 v[46:47], v[46:47], v[30:31]
	v_pk_mul_f32 v[48:49], v[48:49], v[32:33]
	v_pk_mul_f32 v[42:43], v[42:43], v[26:27]
	v_pk_mul_f32 v[44:45], v[44:45], v[28:29]
	v_cvt_pk_fp8_f32 v240, v62, v63
	v_cvt_pk_fp8_f32 v240, v64, v65 op_sel:[0,0,1]
	v_cvt_pk_fp8_f32 v241, v58, v59
	v_cvt_pk_fp8_f32 v241, v60, v61 op_sel:[0,0,1]
	v_cvt_pk_fp8_f32 v242, v46, v47
	v_cvt_pk_fp8_f32 v242, v48, v49 op_sel:[0,0,1]
	v_cvt_pk_fp8_f32 v243, v42, v43
	v_cvt_pk_fp8_f32 v243, v44, v45 op_sel:[0,0,1]
	v_or_b32_e32 v230, v233, v172
	v_ashrrev_i32_e32 v231, 31, v230
	v_lshlrev_b64 v[230:231], 11, v[230:231]
	v_permlane16_swap_b32_e32 v240, v242
	v_permlane16_swap_b32_e32 v241, v243
	v_lshl_add_u64 v[230:231], s[16:17], 0, v[230:231]
	v_lshl_add_u64 v[230:231], v[230:231], 0, v[234:235]
	global_store_dwordx4 v[230:231], v[240:243], off
	v_pk_fma_f32 v[38:39], v[38:39], v[206:207], v[132:133] op_sel_hi:[1,0,1]
	v_pk_fma_f32 v[40:41], v[40:41], v[206:207], v[134:135] op_sel_hi:[1,0,1]
	v_pk_fma_f32 v[34:35], v[34:35], v[206:207], v[136:137] op_sel_hi:[1,0,1]
	v_pk_fma_f32 v[36:37], v[36:37], v[206:207], v[138:139] op_sel_hi:[1,0,1]
	v_pk_fma_f32 v[22:23], v[22:23], v[208:209], v[132:133] op_sel_hi:[1,0,1]
	v_pk_fma_f32 v[24:25], v[24:25], v[208:209], v[134:135] op_sel_hi:[1,0,1]
	v_pk_fma_f32 v[18:19], v[18:19], v[208:209], v[136:137] op_sel_hi:[1,0,1]
	v_pk_fma_f32 v[20:21], v[20:21], v[208:209], v[138:139] op_sel_hi:[1,0,1]
	v_pk_fma_f32 v[14:15], v[14:15], v[206:207], v[140:141] op_sel_hi:[1,0,1]
	v_pk_fma_f32 v[16:17], v[16:17], v[206:207], v[142:143] op_sel_hi:[1,0,1]
	v_pk_fma_f32 v[10:11], v[10:11], v[206:207], v[144:145] op_sel_hi:[1,0,1]
	v_pk_fma_f32 v[12:13], v[12:13], v[206:207], v[146:147] op_sel_hi:[1,0,1]
	v_pk_fma_f32 v[6:7], v[6:7], v[208:209], v[140:141] op_sel_hi:[1,0,1]
	v_pk_fma_f32 v[8:9], v[8:9], v[208:209], v[142:143] op_sel_hi:[1,0,1]
	v_pk_fma_f32 v[2:3], v[2:3], v[208:209], v[144:145] op_sel_hi:[1,0,1]
	v_pk_fma_f32 v[4:5], v[4:5], v[208:209], v[146:147] op_sel_hi:[1,0,1]
	v_min_f32_e32 v38, 0x40e00000, v38
	v_min_f32_e32 v39, 0x40e00000, v39
	v_min_f32_e32 v40, 0x40e00000, v40
	v_min_f32_e32 v41, 0x40e00000, v41
	v_min_f32_e32 v34, 0x40e00000, v34
	v_min_f32_e32 v35, 0x40e00000, v35
	v_min_f32_e32 v36, 0x40e00000, v36
	v_min_f32_e32 v37, 0x40e00000, v37
	v_min_f32_e32 v22, 0x40e00000, v22
	v_min_f32_e32 v23, 0x40e00000, v23
	v_min_f32_e32 v24, 0x40e00000, v24
	v_min_f32_e32 v25, 0x40e00000, v25
	v_min_f32_e32 v18, 0x40e00000, v18
	v_min_f32_e32 v19, 0x40e00000, v19
	v_min_f32_e32 v20, 0x40e00000, v20
	v_min_f32_e32 v21, 0x40e00000, v21
	v_pk_mul_f32 v[210:211], v[38:39], s[98:99] op_sel_hi:[1,0]
	v_pk_mul_f32 v[212:213], v[40:41], s[98:99] op_sel_hi:[1,0]
	v_pk_mul_f32 v[214:215], v[34:35], s[98:99] op_sel_hi:[1,0]
	v_pk_mul_f32 v[216:217], v[36:37], s[98:99] op_sel_hi:[1,0]
	v_pk_mul_f32 v[218:219], v[22:23], s[98:99] op_sel_hi:[1,0]
	v_pk_mul_f32 v[220:221], v[24:25], s[98:99] op_sel_hi:[1,0]
	v_pk_mul_f32 v[222:223], v[18:19], s[98:99] op_sel_hi:[1,0]
	v_pk_mul_f32 v[224:225], v[20:21], s[98:99] op_sel_hi:[1,0]
	v_exp_f32_e32 v210, v210
	v_exp_f32_e32 v211, v211
	v_exp_f32_e32 v212, v212
	v_exp_f32_e32 v213, v213
	v_exp_f32_e32 v214, v214
	v_exp_f32_e32 v215, v215
	v_exp_f32_e32 v216, v216
	v_exp_f32_e32 v217, v217
; __device__ __forceinline__ void swap16(int& x, int& y) { const auto r = __builtin_amdgcn_permlane16_swap((unsigned)x, (unsigned)y, false, false); x = (int)r[0]; y = (int)r[1]; }
; #define PG8_BAR __builtin_amdgcn_s_barrier()
;     __device__ __forceinline__ void operator()(const f32x4 (&acc)[2][2][4][2], const Unit& u, int wr, int wc, int fr, int fq) const {
;     ...
;                     const f32x4 gt = acc[ai][0][m][n] * descale + (n ? g1 : g0), up = acc[ai][1][m][n] * descale + (n ? u1 : u0);
; #pragma unroll
;                     for (int j = 0; j < 4; ++j) { const float g = fminf(gt[j], 7.0f), uu = fminf(fmaxf(up[j], -7.0f), 7.0f);
;                         const float sg = __builtin_amdgcn_rcpf(1.0f + __builtin_amdgcn_exp2f(g * (-1.702f * 1.4426950408889634f)));
;                         o[n][j] = (uu + 1.0f) * (g * sg) * oscale; }
;                 }
;                 w0[m] = __builtin_amdgcn_cvt_pk_fp8_f32(o[0][0], o[0][1], 0, false); w0[m] = __builtin_amdgcn_cvt_pk_fp8_f32(o[0][2], o[0][3], w0[m], true);
;                 w1[m] = __builtin_amdgcn_cvt_pk_fp8_f32(o[1][0], o[1][1], 0, false); w1[m] = __builtin_amdgcn_cvt_pk_fp8_f32(o[1][2], o[1][3], w1[m], true);
;             }
; #pragma unroll
;             for (int p = 0; p < 2; ++p) { swap16(w0[2 * p], w0[2 * p + 1]); swap16(w1[2 * p], w1[2 * p + 1]);
;                 u32x4 w; w.x = (unsigned)w0[2 * p]; w.y = (unsigned)w1[2 * p]; w.z = (unsigned)w0[2 * p + 1]; w.w = (unsigned)w1[2 * p + 1];
;                 *(u32x4*)(ACT + (size_t)(row0 + ai * HALF + (2 * p + odd) * 16) * DFF + colw) = w; }
; template <class Epi, bool GATHER, int MODE, bool SPLIT = false>
; __device__ __forceinline__ void gemm_phase(PG8_LAS unsigned char* lds, const Gemm g, const Order& S, const Epi& E) {
;     ...
;         if (!has_next) break;
; #pragma unroll
;         for (int a = 0; a < 2; ++a)
; #pragma unroll
;             for (int b = 0; b < 2; ++b)
; #pragma unroll
;                 for (int m = 0; m < 4; ++m)
; #pragma unroll
;                     for (int n = 0; n < 2; ++n) acc[a][b][m][n] = (f32x4){0.f, 0.f, 0.f, 0.f};
;         cur = nxt; cB = nB; cAr = nAr; ++ui;
; #pragma unroll
;         for (int h = 0; h < 2; ++h)
; #pragma unroll
;             for (int i = 0; i < 2; ++i) cv[h][i] = nv[h][i];
;         if (wr == 1) PG8_BAR;
	v_exp_f32_e32 v218, v218
	v_exp_f32_e32 v219, v219
	v_exp_f32_e32 v220, v220
	v_exp_f32_e32 v221, v221
	v_exp_f32_e32 v222, v222
	v_exp_f32_e32 v223, v223
	v_exp_f32_e32 v224, v224
	v_exp_f32_e32 v225, v225
	v_med3_f32 v14, v14, s65, v183
	v_med3_f32 v15, v15, s65, v183
	v_med3_f32 v16, v16, s65, v183
	v_med3_f32 v17, v17, s65, v183
	v_med3_f32 v10, v10, s65, v183
	v_med3_f32 v11, v11, s65, v183
	v_med3_f32 v12, v12, s65, v183
	v_med3_f32 v13, v13, s65, v183
	v_med3_f32 v6, v6, s65, v183
	v_med3_f32 v7, v7, s65, v183
	v_med3_f32 v8, v8, s65, v183
	v_med3_f32 v9, v9, s65, v183
	v_med3_f32 v2, v2, s65, v183
	v_med3_f32 v3, v3, s65, v183
	v_med3_f32 v4, v4, s65, v183
	v_med3_f32 v5, v5, s65, v183
	v_pk_add_f32 v[210:211], v[210:211], 1.0 op_sel_hi:[1,0]
	v_pk_add_f32 v[212:213], v[212:213], 1.0 op_sel_hi:[1,0]
	v_pk_add_f32 v[214:215], v[214:215], 1.0 op_sel_hi:[1,0]
	v_pk_add_f32 v[216:217], v[216:217], 1.0 op_sel_hi:[1,0]
	v_pk_add_f32 v[218:219], v[218:219], 1.0 op_sel_hi:[1,0]
	v_pk_add_f32 v[220:221], v[220:221], 1.0 op_sel_hi:[1,0]
	v_pk_add_f32 v[222:223], v[222:223], 1.0 op_sel_hi:[1,0]
	v_pk_add_f32 v[224:225], v[224:225], 1.0 op_sel_hi:[1,0]
	v_rcp_f32_e32 v210, v210
	v_rcp_f32_e32 v211, v211
	v_rcp_f32_e32 v212, v212
	v_rcp_f32_e32 v213, v213
	v_rcp_f32_e32 v214, v214
	v_rcp_f32_e32 v215, v215
	v_rcp_f32_e32 v216, v216
	v_rcp_f32_e32 v217, v217
	v_rcp_f32_e32 v218, v218
	v_rcp_f32_e32 v219, v219
	v_rcp_f32_e32 v220, v220
	v_rcp_f32_e32 v221, v221
	v_rcp_f32_e32 v222, v222
	v_rcp_f32_e32 v223, v223
	v_rcp_f32_e32 v224, v224
	v_rcp_f32_e32 v225, v225
	v_pk_fma_f32 v[14:15], v[14:15], 4.0, 4.0 op_sel_hi:[1,0,0]
	v_pk_fma_f32 v[16:17], v[16:17], 4.0, 4.0 op_sel_hi:[1,0,0]
	v_pk_fma_f32 v[10:11], v[10:11], 4.0, 4.0 op_sel_hi:[1,0,0]
	v_pk_fma_f32 v[12:13], v[12:13], 4.0, 4.0 op_sel_hi:[1,0,0]
	v_pk_fma_f32 v[6:7], v[6:7], 4.0, 4.0 op_sel_hi:[1,0,0]
	v_pk_fma_f32 v[8:9], v[8:9], 4.0, 4.0 op_sel_hi:[1,0,0]
	v_pk_fma_f32 v[2:3], v[2:3], 4.0, 4.0 op_sel_hi:[1,0,0]
	v_pk_fma_f32 v[4:5], v[4:5], 4.0, 4.0 op_sel_hi:[1,0,0]
	v_pk_mul_f32 v[38:39], v[38:39], v[210:211]
	v_pk_mul_f32 v[40:41], v[40:41], v[212:213]
	v_pk_mul_f32 v[34:35], v[34:35], v[214:215]
	v_pk_mul_f32 v[36:37], v[36:37], v[216:217]
	v_pk_mul_f32 v[22:23], v[22:23], v[218:219]
	v_pk_mul_f32 v[24:25], v[24:25], v[220:221]
	v_pk_mul_f32 v[18:19], v[18:19], v[222:223]
	v_pk_mul_f32 v[20:21], v[20:21], v[224:225]
	v_pk_mul_f32 v[38:39], v[38:39], v[14:15]
	v_pk_mul_f32 v[40:41], v[40:41], v[16:17]
	v_pk_mul_f32 v[34:35], v[34:35], v[10:11]
	v_pk_mul_f32 v[36:37], v[36:37], v[12:13]
	v_pk_mul_f32 v[22:23], v[22:23], v[6:7]
	v_pk_mul_f32 v[24:25], v[24:25], v[8:9]
	v_pk_mul_f32 v[18:19], v[18:19], v[2:3]
	v_pk_mul_f32 v[20:21], v[20:21], v[4:5]
	v_cvt_pk_fp8_f32 v244, v38, v39
	v_cvt_pk_fp8_f32 v244, v40, v41 op_sel:[0,0,1]
	v_cvt_pk_fp8_f32 v245, v34, v35
	v_cvt_pk_fp8_f32 v245, v36, v37 op_sel:[0,0,1]
	v_cvt_pk_fp8_f32 v246, v22, v23
	v_cvt_pk_fp8_f32 v246, v24, v25 op_sel:[0,0,1]
	v_cvt_pk_fp8_f32 v247, v18, v19
	v_cvt_pk_fp8_f32 v247, v20, v21 op_sel:[0,0,1]
	v_or_b32_e32 v230, v233, v173
	v_ashrrev_i32_e32 v231, 31, v230
	v_lshlrev_b64 v[230:231], 11, v[230:231]
	v_permlane16_swap_b32_e32 v244, v246
	v_permlane16_swap_b32_e32 v245, v247
	v_lshl_add_u64 v[230:231], s[16:17], 0, v[230:231]
	v_lshl_add_u64 v[230:231], v[230:231], 0, v[234:235]
	global_store_dwordx4 v[230:231], v[244:247], off
	s_and_b64 vcc, exec, s[2:3]
	s_mov_b64 s[0:1], -1
	s_cbranch_vccnz .LBB0_796
	s_andn2_b64 vcc, exec, s[12:13]
	s_cbranch_vccnz .LBB0_795
	s_barrier
	s_branch .LBB0_795
